# split grid barrier (arrive early / wait late) before both router phases so the router weight-table setup overlaps the barrier
# speedup vs baseline: 1.0358x; 1.0008x over previous
.LBB0_843:
	s_cmp_gt_i32 s81, 5
	s_cselect_b64 s[4:5], -1, 0
	s_and_b64 s[0:1], s[0:1], s[4:5]
	s_andn2_b64 vcc, exec, s[0:1]
	s_cbranch_vccnz .LBB0_897
	s_waitcnt vmcnt(0)
	s_waitcnt vmcnt(0)
	s_barrier
	s_and_saveexec_b64 s[0:1], s[78:79]
	s_cbranch_execz .LBB0_896
	v_mov_b32_e32 v1, 0x22160
	s_waitcnt vmcnt(0) lgkmcnt(0)
	ds_read_b32 v2, v1
	v_mov_b32_e32 v3, 1
	v_mov_b32_e32 v4, s99
	v_and_b32_e32 v5, 0xffff, v4
	v_lshrrev_b32_e32 v6, 16, v4
	global_atomic_add v7, v5, v3, s[100:101] sc0
	buffer_inv sc1
	v_lshrrev_b32_e32 v8, 8, v5
	v_sub_u32_e32 v8, s98, v8
	v_add_u32_e32 v8, 7, v8
	v_lshrrev_b32_e32 v8, 3, v8
	v_mov_b32_e32 v9, s98
	v_min_u32_e32 v9, 8, v9
	v_mov_b32_e32 v10, 0
	s_waitcnt lgkmcnt(0)
	v_add_u32_e32 v2, 1, v2
	ds_write_b32 v1, v2
	v_mul_lo_u32 v8, v8, v2
	v_mul_lo_u32 v9, v9, v2
	s_waitcnt vmcnt(0)
	v_add_u32_e32 v7, 1, v7
	v_cmp_eq_u32_e32 vcc, v7, v8
	s_cbranch_vccz .Lgb_done_5
	v_mov_b32_e32 v4, 0
	global_atomic_add v4, v3, s[100:101] offset:2048
	global_atomic_add v4, v3, s[100:101] offset:2304
	global_atomic_add v4, v3, s[100:101] offset:2560
	global_atomic_add v4, v3, s[100:101] offset:2816
	global_atomic_add v4, v3, s[100:101] offset:3072
	global_atomic_add v4, v3, s[100:101] offset:3328
	global_atomic_add v4, v3, s[100:101] offset:3584
	global_atomic_add v4, v3, s[100:101] offset:3840
.Lgb_done_5:
	s_waitcnt lgkmcnt(0)
.LBB0_896:
	s_or_b64 exec, exec, s[0:1]
	s_waitcnt lgkmcnt(0)
.LBB0_897:
	s_cmp_lt_i32 s80, 6
	s_cselect_b64 s[0:1], -1, 0
	s_add_u32 s28, s54, 0x9e00000
	s_addc_u32 s29, s55, 0
	s_add_u32 s24, s54, 0x1780000
	s_addc_u32 s25, s55, 0
	s_and_b64 s[0:1], s[0:1], s[4:5]
	s_andn2_b64 vcc, exec, s[0:1]
	v_lshl_add_u32 v229, v0, 1, 0
	v_lshlrev_b32_e32 v194, 6, v0
	s_cbranch_vccnz .LBB0_944
	v_mov_b32_e32 v195, 0
	v_readlane_b32 s4, v253, 2
	s_waitcnt vmcnt(0)
	v_lshlrev_b32_e32 v22, 2, v0
	v_mov_b32_e32 v23, v195
	v_readlane_b32 s5, v253, 3
	v_readlane_b32 s6, v253, 4
	v_readlane_b32 s7, v253, 5
	v_readlane_b32 s8, v253, 6
	v_readlane_b32 s9, v253, 7
	v_readlane_b32 s10, v253, 8
	v_readlane_b32 s11, v253, 9
	v_readlane_b32 s12, v253, 10
	v_readlane_b32 s13, v253, 11
	v_readlane_b32 s14, v253, 12
	v_readlane_b32 s15, v253, 13
	v_readlane_b32 s16, v253, 14
	v_readlane_b32 s17, v253, 15
	v_readlane_b32 s18, v253, 16
	v_readlane_b32 s19, v253, 17
	v_lshl_add_u64 v[2:3], s[42:43], 0, v[194:195]
	v_lshl_add_u64 v[26:27], s[10:11], 0, v[22:23]
	v_readlane_b32 s4, v253, 18
	v_lshl_add_u64 v[24:25], v[2:3], 0, 32
	v_lshlrev_b32_e32 v2, 4, v0
	v_mov_b32_e32 v3, v195
	v_readlane_b32 s5, v253, 19
	v_readlane_b32 s6, v253, 20
	v_readlane_b32 s7, v253, 21
	v_readlane_b32 s8, v253, 22
	v_readlane_b32 s9, v253, 23
	v_readlane_b32 s10, v253, 24
	v_readlane_b32 s11, v253, 25
	v_readlane_b32 s12, v253, 26
	v_readlane_b32 s18, v253, 32
	v_readlane_b32 s19, v253, 33
	v_or_b32_e32 v1, 0xfffffe00, v0
	v_lshl_add_u32 v30, v0, 1, 0
	v_lshl_add_u64 v[28:29], s[18:19], 0, v[2:3]
	s_mov_b64 s[4:5], 0
	s_movk_i32 s12, 0x7fff
	s_mov_b64 s[6:7], 0x8000
	s_mov_b64 s[8:9], 0x800
	s_mov_b64 s[10:11], 0x2000
	v_readlane_b32 s13, v253, 27
	v_readlane_b32 s14, v253, 28
	v_readlane_b32 s15, v253, 29
	v_readlane_b32 s16, v253, 30
	v_readlane_b32 s17, v253, 31

.LBB0_906:
	s_or_b64 exec, exec, s[8:9]
	s_lshl_b32 s14, s95, 6
	v_or_b32_e32 v2, s14, v222
	v_ashrrev_i32_e32 v3, 31, v2
	v_lshlrev_b64 v[2:3], 11, v[2:3]
	v_and_b32_e32 v1, 48, v0
	v_lshl_add_u64 v[2:3], s[82:83], 0, v[2:3]
	v_lshl_or_b32 v18, s92, 8, v1
	v_mov_b32_e32 v19, 0
	v_lshl_add_u64 v[14:15], v[2:3], 0, v[18:19]
	s_and_saveexec_b64 s[8:9], s[78:79]
	s_cbranch_execz .Lgw_end_5
	v_mov_b32_e32 v1, 0x22160
	ds_read_b32 v2, v1
	v_mov_b32_e32 v3, s99
	v_lshrrev_b32_e32 v4, 16, v3
	v_mov_b32_e32 v5, s98
	v_min_u32_e32 v5, 8, v5
	v_mov_b32_e32 v6, 0
	s_waitcnt lgkmcnt(0)
	v_mul_lo_u32 v5, v5, v2
.Lgw_poll_5:
	global_load_dword v7, v4, s[100:101] sc1
	v_add_u32_e32 v6, 1, v6
	s_waitcnt vmcnt(0)
	v_cmp_ge_u32_e32 vcc, v7, v5
	s_cbranch_vccnz .Lgw_end_5
	v_cmp_gt_u32_e32 vcc, 0x80000, v6
	s_sleep 1
	s_cbranch_vccnz .Lgw_poll_5
.Lgw_end_5:
	s_or_b64 exec, exec, s[8:9]
	s_waitcnt lgkmcnt(0)
	s_barrier
	global_load_dwordx4 v[2:5], v[14:15], off offset:192
	global_load_dwordx4 v[6:9], v[14:15], off offset:128
	global_load_dwordx4 v[10:13], v[14:15], off
	s_nop 0
	global_load_dwordx4 v[14:17], v[14:15], off offset:64
	v_mbcnt_hi_u32_b32 v20, -1, v227
	v_and_b32_e32 v25, 64, v20
	v_and_b32_e32 v36, 0x3f0, v22
	v_xor_b32_e32 v22, 16, v20
	v_lshl_add_u64 v[34:35], s[82:83], 0, v[18:19]
	v_add_u32_e32 v19, 64, v25
	v_lshrrev_b32_e32 v21, 8, v0
	v_bfe_u32 v23, v0, 2, 4
	s_cmp_eq_u32 s95, 0
	v_xor_b32_e32 v26, 32, v20
	v_cmp_lt_i32_e32 vcc, v22, v19
	v_and_b32_e32 v1, 3, v0
	v_or_b32_e32 v24, 16, v222
	v_lshl_or_b32 v23, v21, 4, v23
	v_lshlrev_b32_e32 v39, 10, v21
	s_cselect_b32 s17, 5, 4
	s_and_b32 s12, s87, 0xffffffc0
	s_add_i32 s13, 0, 0x14000
	v_cndmask_b32_e32 v21, v20, v22, vcc
	v_cmp_lt_i32_e32 vcc, v26, v19
	v_and_or_b32 v38, v226, 12, v1
	v_min_u32_e32 v24, 19, v24
	v_add_u32_e32 v18, 0, v18
	s_add_i32 s19, 0, 0x1c400
	v_cndmask_b32_e32 v19, v20, v26, vcc
	s_add_i32 s12, s13, s12
	s_mov_b32 s15, 0
	v_cmp_gt_u32_e64 s[8:9], 16, v208
	v_mov_b32_e32 v37, 0x358637bd
	s_mov_b32 s16, 0x800000
	s_lshl_b32 s18, s92, 11
	v_cmp_eq_u32_e64 s[10:11], 0, v23
	v_lshl_add_u32 v40, v38, 2, s13
	v_lshl_add_u32 v41, v23, 2, s19
	v_lshl_add_u32 v42, v222, 11, v18
	v_lshl_add_u32 v43, v24, 11, v18
	v_lshlrev_b32_e32 v44, 2, v21
	v_lshlrev_b32_e32 v45, 2, v19
	v_lshl_add_u32 v46, v208, 2, s12
	s_waitcnt vmcnt(3)
	v_mov_b32_e32 v50, v2
	v_mov_b32_e32 v49, v3
	v_mov_b32_e32 v48, v4
	v_mov_b32_e32 v47, v5
	s_branch .LBB0_908

.LBB0_1890:
	s_cmp_gt_i32 s81, 12
	s_cselect_b64 s[2:3], -1, 0
	s_and_b64 s[0:1], s[0:1], s[2:3]
	s_andn2_b64 vcc, exec, s[0:1]
	s_cbranch_vccnz .LBB0_1944
	s_waitcnt vmcnt(0)
	s_waitcnt lgkmcnt(0)
	s_barrier
	s_and_saveexec_b64 s[0:1], s[78:79]
	s_cbranch_execz .LBB0_1943
	v_mov_b32_e32 v1, 0x22160
	s_waitcnt vmcnt(0) lgkmcnt(0)
	ds_read_b32 v2, v1
	v_mov_b32_e32 v3, 1
	v_mov_b32_e32 v4, s99
	v_and_b32_e32 v5, 0xffff, v4
	v_lshrrev_b32_e32 v6, 16, v4
	global_atomic_add v7, v5, v3, s[100:101] sc0
	buffer_inv sc1
	v_lshrrev_b32_e32 v8, 8, v5
	v_sub_u32_e32 v8, s98, v8
	v_add_u32_e32 v8, 7, v8
	v_lshrrev_b32_e32 v8, 3, v8
	v_mov_b32_e32 v9, s98
	v_min_u32_e32 v9, 8, v9
	v_mov_b32_e32 v10, 0
	s_waitcnt lgkmcnt(0)
	v_add_u32_e32 v2, 1, v2
	ds_write_b32 v1, v2
	v_mul_lo_u32 v8, v8, v2
	v_mul_lo_u32 v9, v9, v2
	s_waitcnt vmcnt(0)
	v_add_u32_e32 v7, 1, v7
	v_cmp_eq_u32_e32 vcc, v7, v8
	s_cbranch_vccz .Lgb_done_12
	v_mov_b32_e32 v4, 0
	global_atomic_add v4, v3, s[100:101] offset:2048
	global_atomic_add v4, v3, s[100:101] offset:2304
	global_atomic_add v4, v3, s[100:101] offset:2560
	global_atomic_add v4, v3, s[100:101] offset:2816
	global_atomic_add v4, v3, s[100:101] offset:3072
	global_atomic_add v4, v3, s[100:101] offset:3328
	global_atomic_add v4, v3, s[100:101] offset:3584
	global_atomic_add v4, v3, s[100:101] offset:3840
.Lgb_done_12:
	s_waitcnt lgkmcnt(0)
.LBB0_1943:
	s_or_b64 exec, exec, s[0:1]
	s_waitcnt lgkmcnt(0)
.LBB0_1944:
	s_cmp_lt_i32 s80, 13
	s_cselect_b64 s[0:1], -1, 0
	s_and_b64 s[0:1], s[0:1], s[2:3]
	s_andn2_b64 vcc, exec, s[0:1]
	s_cbranch_vccnz .LBB0_1991
	v_mov_b32_e32 v195, 0
	v_readlane_b32 s4, v253, 2
	v_lshl_add_u64 v[2:3], s[38:39], 0, v[194:195]
	s_mov_b64 s[2:3], 0x10030
	v_lshlrev_b32_e32 v22, 2, v0
	v_mov_b32_e32 v23, v195
	v_readlane_b32 s5, v253, 3
	v_readlane_b32 s6, v253, 4
	v_readlane_b32 s7, v253, 5
	v_readlane_b32 s8, v253, 6
	v_readlane_b32 s9, v253, 7
	v_readlane_b32 s10, v253, 8
	v_readlane_b32 s11, v253, 9
	v_readlane_b32 s12, v253, 10
	v_readlane_b32 s13, v253, 11
	v_readlane_b32 s14, v253, 12
	v_readlane_b32 s15, v253, 13
	v_readlane_b32 s16, v253, 14
	v_readlane_b32 s17, v253, 15
	v_readlane_b32 s18, v253, 16
	v_readlane_b32 s19, v253, 17
	v_lshl_add_u64 v[24:25], v[2:3], 0, s[2:3]
	v_lshl_add_u64 v[2:3], s[10:11], 0, v[22:23]
	v_readlane_b32 s4, v253, 18
	s_mov_b64 s[2:3], 0x1000
	v_mov_b32_e32 v251, v195
	v_readlane_b32 s18, v253, 32
	v_readlane_b32 s19, v253, 33
	v_lshl_add_u64 v[26:27], v[2:3], 0, s[2:3]
	v_readlane_b32 s5, v253, 19
	v_readlane_b32 s6, v253, 20
	v_readlane_b32 s7, v253, 21
	v_readlane_b32 s8, v253, 22
	v_readlane_b32 s9, v253, 23
	v_readlane_b32 s10, v253, 24
	v_lshl_add_u64 v[2:3], s[18:19], 0, v[250:251]
	s_mov_b64 s[2:3], 0x4000
	v_or_b32_e32 v1, 0xfffffe00, v0
	v_lshl_add_u64 v[28:29], v[2:3], 0, s[2:3]
	s_mov_b64 s[2:3], 0
	s_movk_i32 s10, 0x7fff
	s_mov_b64 s[4:5], 0x8000
	s_mov_b64 s[6:7], 0x800
	s_mov_b64 s[8:9], 0x2000
	v_readlane_b32 s11, v253, 25
	v_readlane_b32 s12, v253, 26
	v_readlane_b32 s13, v253, 27
	v_readlane_b32 s14, v253, 28
	v_readlane_b32 s15, v253, 29
	v_readlane_b32 s16, v253, 30
	v_readlane_b32 s17, v253, 31

.LBB0_1953:
	s_or_b64 exec, exec, s[2:3]
	s_lshl_b32 s16, s95, 6
	v_or_b32_e32 v18, s16, v222
	v_ashrrev_i32_e32 v19, 31, v18
	v_lshlrev_b64 v[2:3], 11, v[18:19]
	v_and_b32_e32 v1, 48, v0
	v_lshl_add_u64 v[2:3], s[82:83], 0, v[2:3]
	v_lshl_or_b32 v20, s92, 8, v1
	v_mov_b32_e32 v21, 0
	v_lshl_add_u64 v[24:25], v[2:3], 0, v[20:21]
	s_and_saveexec_b64 s[8:9], s[78:79]
	s_cbranch_execz .Lgw_end_12
	v_mov_b32_e32 v1, 0x22160
	ds_read_b32 v2, v1
	v_mov_b32_e32 v3, s99
	v_lshrrev_b32_e32 v4, 16, v3
	v_mov_b32_e32 v5, s98
	v_min_u32_e32 v5, 8, v5
	v_mov_b32_e32 v6, 0
	s_waitcnt lgkmcnt(0)
	v_mul_lo_u32 v5, v5, v2

.Lgw_end_12:
	s_or_b64 exec, exec, s[8:9]
	s_waitcnt lgkmcnt(0)
	s_barrier
	global_load_dwordx4 v[2:5], v[24:25], off offset:192
	global_load_dwordx4 v[6:9], v[24:25], off offset:128
	global_load_dwordx4 v[10:13], v[24:25], off
	global_load_dwordx4 v[14:17], v[24:25], off offset:64
	v_mbcnt_hi_u32_b32 v19, -1, v227
	v_and_b32_e32 v1, 3, v0
	v_and_b32_e32 v27, 64, v19
	v_lshrrev_b32_e32 v23, 8, v0
	v_bfe_u32 v24, v0, 2, 4
	v_and_b32_e32 v38, 0x3f0, v22
	v_bfe_u32 v22, v0, 6, 2
	v_xor_b32_e32 v26, 16, v19
	v_lshlrev_b32_e32 v31, 2, v1
	v_lshlrev_b32_e32 v32, 7, v1
	v_lshl_add_u64 v[34:35], s[82:83], 0, v[20:21]
	v_add_u32_e32 v21, 64, v27
	v_or_b32_e32 v25, 16, v222
	v_xor_b32_e32 v28, 32, v19
	v_lshl_or_b32 v30, v23, 4, v24
	v_lshlrev_b32_e32 v40, 10, v23
	v_lshlrev_b32_e32 v23, 6, v23
	v_lshlrev_b32_e32 v24, 2, v24
	v_lshl_or_b32 v27, v22, 4, v31
	v_lshl_or_b32 v22, v22, 9, v32
	v_cmp_lt_i32_e32 vcc, v26, v21
	s_and_b32 s2, s77, 0xffffffc0
	s_add_i32 s3, 0, 0x14000
	v_min_u32_e32 v25, 19, v25
	v_add_u32_e32 v20, 0, v20
	v_or_b32_e32 v36, 16, v18
	v_cndmask_b32_e32 v18, v19, v26, vcc
	v_cmp_lt_i32_e32 vcc, v28, v21
	v_or3_b32 v21, v22, v23, v24
	s_add_i32 s2, s3, s2
	v_and_or_b32 v29, v226, 12, v1
	v_cndmask_b32_e32 v19, v19, v28, vcc
	v_lshl_add_u32 v43, v222, 11, v20
	v_lshl_add_u32 v44, v25, 11, v20
	v_add_u32_e32 v20, 0, v27
	v_lshlrev_b32_e32 v45, 2, v18
	v_add_u32_e32 v18, 0, v21
	s_mov_b32 s12, 0
	v_cmp_gt_u32_e64 s[8:9], 16, v82
	s_lshl_b32 s13, s92, 11
	v_mov_b32_e32 v39, 0x358637bd
	s_mov_b32 s14, 0x800000
	s_mov_b32 s15, 0
	v_lshl_add_u32 v41, v82, 2, s2
	v_lshl_add_u32 v42, v29, 2, s3
	v_cmp_eq_u32_e64 s[10:11], 0, v30
	v_lshlrev_b32_e32 v46, 2, v19
	v_add_u32_e32 v47, 0x1ec00, v20
	v_add_u32_e32 v48, 0x1c400, v18
	s_waitcnt vmcnt(3)
	v_mov_b32_e32 v52, v2
	v_mov_b32_e32 v51, v3
	v_mov_b32_e32 v50, v4
	v_mov_b32_e32 v49, v5
	s_branch .LBB0_1955
